# conversion pools repartitioned: prologue converts layer-0 weights only, layer-1 weights converted in the idle half round of dense-up, FFN+expert items split 4112/4112 across the two attention phases
# speedup vs baseline: 1.0075x; 1.0075x over previous
.LBB0_28:
	s_or_b64 exec, exec, s[2:3]
	s_add_u32 s4, s94, 0x9c00000
	s_addc_u32 s5, s95, 0
	s_add_u32 s6, s94, 0x7000000
	s_addc_u32 s7, s95, 0
	s_add_u32 s33, s94, 0x6000000
	s_addc_u32 s52, s95, 0
	s_add_u32 s53, s94, 0x5800000
	s_addc_u32 s54, s95, 0
	s_add_u32 s55, s94, 0x5000000
	s_addc_u32 s56, s95, 0
	s_add_u32 s57, s94, 0x800000
	s_addc_u32 s58, s95, 0
	s_add_i32 s2, 0, 0x20180
	v_mov_b32_e32 v1, s2
	s_waitcnt lgkmcnt(0)
	s_waitcnt lgkmcnt(0)
	s_barrier
	ds_read_b32 v3, v1
	s_movk_i32 s3, 0x33f
	v_lshrrev_b32_e32 v1, 1, v0
	s_movk_i32 s2, 0x340
	v_and_b32_e32 v1, 0xf0, v1
	s_waitcnt lgkmcnt(0)
	v_cmp_lt_i32_e32 vcc, s3, v3
	v_and_b32_e32 v75, 0x7c, v2
	v_readfirstlane_b32 s13, v3
	v_cmp_gt_i32_e64 s[2:3], s2, v3
	s_cbranch_vccnz .LBB0_34
	s_cmpk_gt_i32 s13, 0x67f
	s_cbranch_scc0 .LBB0_35
	s_cmpk_gt_u32 s13, 0x7df
	s_cbranch_scc0 .LBB0_36
	s_cmpk_gt_u32 s13, 0x93f
	s_cbranch_scc0 .LBB0_44
	s_add_i32 s12, s13, 0xfffff6c0
	s_mov_b64 s[10:11], s[82:83]
	s_mov_b32 s27, 1
	s_cbranch_execz .LBB0_45
	s_movk_i32 s14, 0x800
	s_mov_b32 s26, 0
	s_movk_i32 s25, 0x1600
	s_mov_b64 s[68:69], s[4:5]
	s_cbranch_execz .LBB0_37
	s_branch .LBB0_38

.LBB0_57:
	v_lshlrev_b32_e32 v68, 4, v0
	v_lshrrev_b32_e32 v76, 5, v0
	v_and_b32_e32 v66, 31, v0
	v_and_b32_e32 v67, 0x1e0, v0
	v_lshrrev_b32_e32 v79, 4, v0
	v_and_b32_e32 v70, 0xf0, v68
	v_add_u32_e32 v67, 0, v67
	v_mul_u32_u24_e32 v77, 0x840, v66
	v_add_u32_e32 v68, 0, v70
	v_mov_b32_e32 v73, 0
	v_mul_u32_u24_e32 v69, 0x210, v79
	v_lshl_add_u32 v72, v66, 4, 0
	v_lshlrev_b32_e32 v74, 3, v66
	v_mul_u32_u24_e32 v66, 0x210, v76
	s_mov_b32 s11, 0
	v_lshl_add_u32 v78, v76, 4, 0
	v_mov_b32_e32 v71, v73
	v_or_b32_e32 v80, 64, v79
	v_or_b32_e32 v81, 32, v76
	v_or_b32_e32 v82, 64, v76
	v_or_b32_e32 v83, 0x60, v76
	s_mov_b32 s12, 0x7ffffffe
	s_mov_b32 s13, 0xc2fe0000
	s_mov_b32 s14, 0x4b400000
	v_add_u32_e32 v84, v67, v77
	s_add_i32 s15, 0, 0x20184
	s_movk_i32 s20, 0x33f
	v_mov_b32_e32 v85, 0x42fe0000
	v_add_u32_e32 v86, v68, v69
	v_add_u32_e32 v87, v72, v66
	s_branch .LBB0_60

.LBB0_75:
	v_mov_b32_e32 v66, 0x340

.LBB0_486:
	s_or_b64 exec, exec, s[6:7]
	s_waitcnt vmcnt(0)
	v_readfirstlane_b32 s6, v3
	s_nop 1
	v_add_u32_e32 v2, s6, v2
	s_add_i32 s6, 0, 0x20180
	v_add_u32_e32 v2, 0x680, v2
	v_mov_b32_e32 v3, s6
	ds_write_b32 v3, v2
.LBB0_487:
	s_or_b64 exec, exec, s[2:3]
	s_add_i32 s2, 0, 0x20180
	v_mov_b32_e32 v2, s2
	s_waitcnt lgkmcnt(0)
	s_waitcnt lgkmcnt(0)
	s_barrier
	ds_read_b32 v2, v2
	s_movk_i32 s3, 0x168f
	s_movk_i32 s2, 0x1690
	s_waitcnt lgkmcnt(0)
	v_cmp_lt_i32_e32 vcc, s3, v2
	v_readfirstlane_b32 s12, v2
	v_cmp_gt_i32_e64 s[2:3], s2, v2
	s_cbranch_vccnz .LBB0_493
	s_cmpk_gt_i32 s12, 0x67f
	s_cbranch_scc0 .LBB0_494
	s_cmpk_gt_u32 s12, 0xa9f
	s_cbranch_scc0 .LBB0_495
	s_add_i32 s6, s12, 0xfffff560
	s_bfe_u32 s7, s6, 0x100007
	s_mulk_i32 s7, 0x2493
	s_lshr_b32 s17, s7, 16
	s_mul_i32 s16, s17, 0xfffffc80
	s_add_i32 s16, s16, s6
	s_cmpk_gt_i32 s16, 0x1bf
	s_mul_hi_u32 s19, s17, 0x3800000
	s_mul_i32 s20, s17, 0x3800000
	s_cbranch_scc0 .LBB0_496
	s_cmpk_gt_u32 s16, 0x37f
	s_cbranch_scc0 .LBB0_497
	s_add_i32 s10, s16, 0xfffffc80
	s_add_u32 s6, s26, s20
	s_addc_u32 s7, s27, s19
	s_mul_i32 s11, s17, 0xe00000
	s_add_u32 s11, s30, s11
	s_addc_u32 s13, s31, 0
	s_add_u32 s82, s11, 0x27200000
	s_addc_u32 s83, s13, 0
	s_mov_b64 s[28:29], 0
	s_branch .LBB0_498

.LBB0_549:
	s_cmp_gt_u32 s16, 20
	v_mov_b32_e32 v66, 0x1690
	s_cbranch_scc1 .LBB0_553
	s_mov_b64 s[30:31], exec
	v_mbcnt_lo_u32_b32 v66, s30, 0
	v_mbcnt_hi_u32_b32 v66, s31, v66
	v_cmp_eq_u32_e32 vcc, 0, v66
	s_and_saveexec_b64 s[28:29], vcc
	s_cbranch_execz .LBB0_552
	s_bcnt1_i32_b64 s11, s[30:31]
	v_readlane_b32 s36, v254, 38
	v_mov_b32_e32 v67, s11
	v_readlane_b32 s50, v254, 52
	v_readlane_b32 s51, v254, 53
	v_readlane_b32 s37, v254, 39
	v_readlane_b32 s38, v254, 40
	v_readlane_b32 s39, v254, 41
	v_readlane_b32 s40, v254, 42
	v_readlane_b32 s41, v254, 43
	global_atomic_add v67, v75, v67, s[50:51] offset:1280 sc0
	v_readlane_b32 s42, v254, 44
	v_readlane_b32 s43, v254, 45
	v_readlane_b32 s44, v254, 46
	v_readlane_b32 s45, v254, 47
	v_readlane_b32 s46, v254, 48
	v_readlane_b32 s47, v254, 49
	v_readlane_b32 s48, v254, 50
	v_readlane_b32 s49, v254, 51
.LBB0_552:
	s_or_b64 exec, exec, s[28:29]
	s_waitcnt vmcnt(0)
	v_readfirstlane_b32 s11, v67
	s_nop 1
	v_add_u32_e32 v66, s11, v66
	v_add_u32_e32 v66, 0x680, v66

.LBB0_554:
	s_or_b64 exec, exec, s[2:3]
	v_mov_b32_e32 v66, s67
	s_waitcnt lgkmcnt(0)
	s_waitcnt lgkmcnt(0)
	s_barrier
	ds_read_b32 v66, v66
	s_movk_i32 s2, 0x168f
	s_mov_b64 s[82:83], s[80:81]
	s_mov_b32 s11, s68
	s_mov_b32 s18, s12
	s_waitcnt lgkmcnt(0)
	v_cmp_lt_i32_e64 s[2:3], s2, v66
	v_readfirstlane_b32 s23, v66
	s_and_b64 vcc, exec, s[2:3]
	s_mov_b32 s13, s69
	s_mov_b32 s21, s78
	s_mov_b32 s84, s10
	s_mov_b32 s20, s19
	s_cbranch_vccnz .LBB0_591
	s_cmpk_gt_i32 s23, 0x67f
	s_mov_b64 s[28:29], -1
	s_cbranch_scc0 .LBB0_576
	s_cmpk_gt_u32 s23, 0xa9f
	s_cbranch_scc0 .LBB0_565
	s_add_i32 s11, s23, 0xfffff560
	s_bfe_u32 s13, s11, 0x100007
	s_mulk_i32 s13, 0x2493
	s_lshr_b32 s21, s13, 16
	s_mul_i32 s20, s21, 0xfffffc80
	s_add_i32 s20, s20, s11
	s_cmpk_gt_i32 s20, 0x1bf
	s_mul_hi_u32 s24, s21, 0x3800000
	s_mul_i32 s25, s21, 0x3800000
	s_cbranch_scc0 .LBB0_562
	s_cmpk_gt_u32 s20, 0x37f
	s_cbranch_scc0 .LBB0_560
	v_readlane_b32 s36, v254, 38
	s_add_i32 s22, s20, 0xfffffc80
	v_readlane_b32 s46, v254, 48
	v_readlane_b32 s47, v254, 49
	s_add_u32 s34, s46, s25
	s_addc_u32 s35, s47, s24
	s_mul_i32 s11, s21, 0xe00000
	s_add_u32 s82, s17, s11
	v_readlane_b32 s37, v254, 39
	v_readlane_b32 s38, v254, 40
	v_readlane_b32 s39, v254, 41
	v_readlane_b32 s40, v254, 42
	v_readlane_b32 s41, v254, 43
	v_readlane_b32 s42, v254, 44
	v_readlane_b32 s43, v254, 45
	v_readlane_b32 s44, v254, 46
	v_readlane_b32 s45, v254, 47
	v_readlane_b32 s48, v254, 50
	v_readlane_b32 s49, v254, 51
	v_readlane_b32 s50, v254, 52
	v_readlane_b32 s51, v254, 53
	s_addc_u32 s83, s53, 0
	s_mov_b64 s[28:29], 0

.LBB0_728:
	s_or_b64 exec, exec, s[4:5]
	s_waitcnt vmcnt(0)
	v_readfirstlane_b32 s4, v3
	s_nop 1
	v_add_u32_e32 v2, s4, v2
	s_add_i32 s4, 0, 0x20180
	v_add_u32_e32 v2, 0x680, v2
	v_mov_b32_e32 v3, s4
	ds_write_b32 v3, v2
.LBB0_729:
	s_or_b64 exec, exec, s[2:3]
	s_add_i32 s2, 0, 0x20180
	s_waitcnt vmcnt(15)
	v_mov_b32_e32 v2, s2
	s_waitcnt lgkmcnt(0)
	s_waitcnt lgkmcnt(0)
	s_barrier
	ds_read_b32 v2, v2
	s_movk_i32 s3, 0x168f
	s_movk_i32 s2, 0x1690
	s_waitcnt lgkmcnt(0)
	v_cmp_lt_i32_e32 vcc, s3, v2
	v_readfirstlane_b32 s12, v2
	v_cmp_gt_i32_e64 s[2:3], s2, v2
	s_cbranch_vccnz .LBB0_735
	s_cmpk_gt_i32 s12, 0x67f
	s_cbranch_scc0 .LBB0_736
	s_cmpk_gt_u32 s12, 0xa9f
	s_cbranch_scc0 .LBB0_737
	s_add_i32 s4, s12, 0xfffff560
	s_bfe_u32 s5, s4, 0x100007
	s_mulk_i32 s5, 0x2493
	s_lshr_b32 s19, s5, 16
	s_mul_i32 s17, s19, 0xfffffc80
	s_add_i32 s17, s17, s4
	s_cmpk_gt_i32 s17, 0x1bf
	s_mul_hi_u32 s20, s19, 0x3800000
	s_mul_i32 s21, s19, 0x3800000
	s_cbranch_scc0 .LBB0_738
	s_cmpk_gt_u32 s17, 0x37f
	s_cbranch_scc0 .LBB0_739
	s_add_i32 s10, s17, 0xfffffc80
	s_add_u32 s4, s46, s21
	s_addc_u32 s5, s47, s20
	s_mul_i32 s6, s19, 0xe00000
	s_add_u32 s6, s50, s6
	s_addc_u32 s7, s51, 0
	s_add_u32 s80, s6, 0x27200000
	s_addc_u32 s81, s7, 0
	s_mov_b64 s[6:7], 0
	s_branch .LBB0_740

.LBB0_790:
	s_cmp_ge_u32 s17, s16
	v_mov_b32_e32 v66, 0x1690
	s_cbranch_scc1 .LBB0_794
	s_mov_b64 s[30:31], exec
	v_mbcnt_lo_u32_b32 v66, s30, 0
	v_mbcnt_hi_u32_b32 v66, s31, v66
	v_cmp_eq_u32_e32 vcc, 0, v66
	s_and_saveexec_b64 s[28:29], vcc
	s_cbranch_execz .LBB0_793
	s_bcnt1_i32_b64 s11, s[30:31]
	v_mov_b32_e32 v67, s11
	global_atomic_add v67, v71, v67, s[50:51] offset:1280 sc0

.LBB0_795:
	s_or_b64 exec, exec, s[2:3]
	v_mov_b32_e32 v66, s65
	s_waitcnt lgkmcnt(0)
	s_waitcnt lgkmcnt(0)
	s_barrier
	ds_read_b32 v66, v66
	s_movk_i32 s2, 0x168f
	s_mov_b64 s[80:81], s[78:79]
	s_mov_b32 s11, s66
	s_mov_b32 s18, s12
	s_waitcnt lgkmcnt(0)
	v_cmp_lt_i32_e64 s[2:3], s2, v66
	v_readfirstlane_b32 s23, v66
	s_and_b64 vcc, exec, s[2:3]
	s_mov_b32 s13, s67
	s_mov_b32 s21, s74
	s_mov_b32 s82, s10
	s_mov_b32 s20, s19
	s_cbranch_vccnz .LBB0_832
	s_cmpk_gt_i32 s23, 0x67f
	s_mov_b64 s[28:29], -1
	s_cbranch_scc0 .LBB0_817
	s_cmpk_gt_u32 s23, 0xa9f
	s_cbranch_scc0 .LBB0_806
	s_add_i32 s11, s23, 0xfffff560
	s_bfe_u32 s13, s11, 0x100007
	s_mulk_i32 s13, 0x2493
	s_lshr_b32 s21, s13, 16
	s_mul_i32 s20, s21, 0xfffffc80
	s_add_i32 s20, s20, s11
	s_cmpk_gt_i32 s20, 0x1bf
	s_mul_hi_u32 s24, s21, 0x3800000
	s_mul_i32 s25, s21, 0x3800000
	s_cbranch_scc0 .LBB0_803
	s_cmpk_gt_u32 s20, 0x37f
	s_cbranch_scc0 .LBB0_801
	v_readlane_b32 s36, v254, 38
	s_add_i32 s22, s20, 0xfffffc80
	v_readlane_b32 s46, v254, 48
	v_readlane_b32 s47, v254, 49
	s_add_u32 s34, s46, s25
	s_addc_u32 s35, s47, s24
	s_mul_i32 s11, s21, 0xe00000
	s_add_u32 s80, s33, s11
	v_readlane_b32 s37, v254, 39
	v_readlane_b32 s38, v254, 40
	v_readlane_b32 s39, v254, 41
	v_readlane_b32 s40, v254, 42
	v_readlane_b32 s41, v254, 43
	v_readlane_b32 s42, v254, 44
	v_readlane_b32 s43, v254, 45
	v_readlane_b32 s44, v254, 46
	v_readlane_b32 s45, v254, 47
	v_readlane_b32 s48, v254, 50
	v_readlane_b32 s49, v254, 51
	v_readlane_b32 s50, v254, 52
	v_readlane_b32 s51, v254, 53
	s_addc_u32 s81, s52, 0
	s_mov_b64 s[28:29], 0

.LBB0_1023:
	s_or_b64 exec, exec, s[2:3]
	s_add_i32 s2, 0, 0x20180
	v_mov_b32_e32 v2, s2
	s_waitcnt lgkmcnt(0)
	s_waitcnt lgkmcnt(0)
	s_barrier
	ds_read_b32 v2, v2
	s_movk_i32 s3, 0x168f
	s_movk_i32 s2, 0x1690
	s_waitcnt lgkmcnt(0)
	v_cmp_lt_i32_e32 vcc, s3, v2
	v_readfirstlane_b32 s11, v2
	v_cmp_gt_i32_e64 s[2:3], s2, v2
	s_cbranch_vccnz .LBB0_1029
	s_cmpk_gt_i32 s11, 0x67f
	s_cbranch_scc0 .LBB0_1030
	s_cmpk_gt_u32 s11, 0xa9f
	s_cbranch_scc0 .LBB0_1031
	s_add_i32 s4, s11, 0xfffff560
	s_bfe_u32 s5, s4, 0x100007
	s_mulk_i32 s5, 0x2493
	s_lshr_b32 s13, s5, 16
	s_mul_i32 s12, s13, 0xfffffc80
	s_add_i32 s12, s12, s4
	s_cmpk_gt_i32 s12, 0x1bf
	s_mul_hi_u32 s16, s13, 0x3800000
	s_mul_i32 s17, s13, 0x3800000
	s_cbranch_scc0 .LBB0_1033
	s_cmpk_gt_u32 s12, 0x37f
	s_cbranch_scc0 .LBB0_1034
	s_add_i32 s10, s12, 0xfffffc80
	s_add_u32 s4, s26, s17
	s_addc_u32 s5, s27, s16
	s_mul_i32 s6, s13, 0xe00000
	s_add_u32 s6, s30, s6
	s_addc_u32 s7, s31, 0
	s_add_u32 s80, s6, 0x27200000
	s_addc_u32 s81, s7, 0
	s_mov_b64 s[6:7], 0
	s_branch .LBB0_1035

.LBB0_1087:
	s_or_b64 exec, exec, s[28:29]
	s_waitcnt vmcnt(0)
	v_readfirstlane_b32 s18, v67
	s_nop 1
	v_add_u32_e32 v66, s18, v66
	v_add_u32_e32 v66, 0x680, v66
	s_branch .LBB0_1089
.LBB0_1088:
	v_mov_b32_e32 v66, 0x1690

.LBB0_1090:
	s_or_b64 exec, exec, s[2:3]
	v_mov_b32_e32 v66, s64
	s_waitcnt lgkmcnt(0)
	s_waitcnt lgkmcnt(0)
	s_barrier
	ds_read_b32 v66, v66
	s_movk_i32 s2, 0x168f
	s_mov_b64 s[80:81], s[78:79]
	s_mov_b32 s18, s10
	s_mov_b32 s20, s12
	s_waitcnt lgkmcnt(0)
	v_cmp_lt_i32_e64 s[2:3], s2, v66
	v_readfirstlane_b32 s25, v66
	s_and_b64 vcc, exec, s[2:3]
	s_mov_b32 s19, s11
	s_mov_b32 s23, s74
	s_mov_b32 s82, s13
	s_mov_b32 s21, s22
	s_cbranch_vccnz .LBB0_1127
	s_cmpk_gt_i32 s25, 0x67f
	s_mov_b64 s[28:29], -1
	s_cbranch_scc0 .LBB0_1112
	s_cmpk_gt_u32 s25, 0xa9f
	s_cbranch_scc0 .LBB0_1101
	s_add_i32 s18, s25, 0xfffff560
	s_bfe_u32 s19, s18, 0x100007
	s_mulk_i32 s19, 0x2493
	s_lshr_b32 s23, s19, 16
	s_mul_i32 s21, s23, 0xfffffc80
	s_add_i32 s21, s21, s18
	s_cmpk_gt_i32 s21, 0x1bf
	s_mul_hi_u32 s26, s23, 0x3800000
	s_mul_i32 s27, s23, 0x3800000
	s_cbranch_scc0 .LBB0_1098
	s_cmpk_gt_u32 s21, 0x37f
	s_cbranch_scc0 .LBB0_1096
	v_readlane_b32 s36, v254, 38
	s_add_i32 s24, s21, 0xfffffc80
	v_readlane_b32 s46, v254, 48
	v_readlane_b32 s47, v254, 49
	s_add_u32 s34, s46, s27
	s_addc_u32 s35, s47, s26
	s_mul_i32 s18, s23, 0xe00000
	s_add_u32 s80, s16, s18
	v_readlane_b32 s37, v254, 39
	v_readlane_b32 s38, v254, 40
	v_readlane_b32 s39, v254, 41
	v_readlane_b32 s40, v254, 42
	v_readlane_b32 s41, v254, 43
	v_readlane_b32 s42, v254, 44
	v_readlane_b32 s43, v254, 45
	v_readlane_b32 s44, v254, 46
	v_readlane_b32 s45, v254, 47
	v_readlane_b32 s48, v254, 50
	v_readlane_b32 s49, v254, 51
	v_readlane_b32 s50, v254, 52
	v_readlane_b32 s51, v254, 53
	s_addc_u32 s81, s17, 0
	s_mov_b64 s[28:29], 0

.LBB0_1511:
	s_or_b64 exec, exec, s[12:13]
	s_waitcnt vmcnt(0)
	v_readfirstlane_b32 s10, v3
	s_nop 1
	v_add_u32_e32 v2, s10, v2
	s_add_i32 s10, 0, 0x20180
	v_add_u32_e32 v2, 0x340, v2
	v_mov_b32_e32 v3, s10
	ds_write_b32 v3, v2
.LBB0_1512:
	s_or_b64 exec, exec, s[2:3]
	s_add_i32 s2, 0, 0x20180
	s_waitcnt vmcnt(15)
	v_mov_b32_e32 v2, s2
	s_waitcnt lgkmcnt(0)
	s_waitcnt lgkmcnt(0)
	s_barrier
	ds_read_b32 v2, v2
	s_movk_i32 s3, 0x67f
	s_movk_i32 s2, 0x680
	s_waitcnt lgkmcnt(0)
	v_cmp_lt_i32_e32 vcc, s3, v2
	v_readfirstlane_b32 s11, v2
	v_cmp_gt_i32_e64 s[2:3], s2, v2
	s_cbranch_vccnz .LBB0_1517
	s_cmpk_gt_i32 s11, 0x67f
	s_cbranch_scc0 .LBB0_1518
	s_cmpk_gt_u32 s11, 0xa9f
	s_cbranch_scc0 .LBB0_1519
	s_add_i32 s16, s11, 0xfffff560
	s_cmpk_gt_u32 s16, 0x1bf
	s_cbranch_scc0 .LBB0_1521
	s_add_i32 s10, s11, 0xfffff3a0
	s_add_u32 s86, s50, 0xb200000
	s_addc_u32 s87, s51, 0
	s_mov_b64 s[28:29], 0
	s_mov_b64 s[12:13], s[44:45]
	s_branch .LBB0_1522

.LBB0_1551:
	v_readlane_b32 s36, v254, 38
	s_and_b64 s[2:3], s[6:7], exec
	v_readlane_b32 s50, v254, 52
	s_cselect_b32 s17, 0x7fffffff, 7
	v_readlane_b32 s51, v254, 53
	s_add_u32 s12, s50, 0xb200000
	s_addc_u32 s13, s51, 0
	s_add_u32 s78, s50, 0x9c00000
	s_addc_u32 s79, s51, 0
	s_add_u32 s18, s50, 0x6000000
	s_addc_u32 s19, s51, 0
	s_add_u32 s20, s50, 0x5800000
	s_addc_u32 s10, s51, 0
	s_add_u32 s11, s50, 0x5000000
	v_lshrrev_b32_e32 v75, 5, v0
	v_and_b32_e32 v67, 31, v0
	v_and_b32_e32 v66, 0x1e0, v0
	v_lshrrev_b32_e32 v81, 4, v0
	v_and_b32_e32 v72, 0xf0, v1
	s_addc_u32 s21, s51, 0
	v_add_u32_e32 v68, 0, v66
	v_mul_u32_u24_e32 v78, 0x840, v67
	v_and_b32_e32 v66, 0x7c, v145
	v_mov_b32_e32 v71, 0
	v_add_u32_e32 v69, 0, v72
	v_mul_u32_u24_e32 v76, 0x210, v81
	v_lshl_add_u32 v77, v67, 4, 0
	v_lshlrev_b32_e32 v74, 3, v67
	v_mul_u32_u24_e32 v67, 0x210, v75
	s_add_u32 s22, s50, 0x800000
	s_mov_b32 s7, 0
	v_lshl_add_u32 v79, v75, 4, 0
	v_and_b32_e32 v80, 0xf0, v144
	v_mov_b32_e32 v73, v71
	v_or_b32_e32 v1, 64, v81
	v_or_b32_e32 v82, 32, v75
	v_or_b32_e32 v83, 64, v75
	v_or_b32_e32 v84, 0x60, v75
	s_addc_u32 s23, s51, 0
	s_mov_b32 s24, 0xc2fe0000
	s_mov_b32 s80, 0x4b400000
	v_add_u32_e32 v85, v68, v78
	s_add_i32 s25, 0, 0x20184
	v_lshlrev_b32_e32 v70, 2, v66
	v_mov_b32_e32 v86, 0x42fe0000
	v_add_u32_e32 v87, v69, v76
	v_add_u32_e32 v88, v77, v67
	v_readlane_b32 s37, v254, 39
	v_readlane_b32 s38, v254, 40
	v_readlane_b32 s39, v254, 41
	v_readlane_b32 s40, v254, 42
	v_readlane_b32 s41, v254, 43
	v_readlane_b32 s42, v254, 44
	v_readlane_b32 s43, v254, 45
	v_readlane_b32 s44, v254, 46
	v_readlane_b32 s45, v254, 47
	v_readlane_b32 s46, v254, 48
	v_readlane_b32 s47, v254, 49
	v_readlane_b32 s48, v254, 50
	v_readlane_b32 s49, v254, 51
	s_branch .LBB0_1554

.LBB0_1565:
	s_cmp_ge_u32 s16, s17
	v_mov_b32_e32 v66, 0x680
	s_cbranch_scc1 .LBB0_1569
	s_mov_b64 s[30:31], exec
	v_mbcnt_lo_u32_b32 v66, s30, 0
	v_mbcnt_hi_u32_b32 v66, s31, v66
	v_cmp_eq_u32_e32 vcc, 0, v66
	s_and_saveexec_b64 s[28:29], vcc
	s_cbranch_execz .LBB0_1568
	s_bcnt1_i32_b64 s6, s[30:31]
	v_readlane_b32 s36, v254, 38
	v_mov_b32_e32 v67, s6
	v_readlane_b32 s50, v254, 52
	v_readlane_b32 s51, v254, 53
	v_readlane_b32 s37, v254, 39
	v_readlane_b32 s38, v254, 40
	v_readlane_b32 s39, v254, 41
	v_readlane_b32 s40, v254, 42
	v_readlane_b32 s41, v254, 43
	global_atomic_add v67, v71, v67, s[50:51] offset:1024 sc0
	v_readlane_b32 s42, v254, 44
	v_readlane_b32 s43, v254, 45
	v_readlane_b32 s44, v254, 46
	v_readlane_b32 s45, v254, 47
	v_readlane_b32 s46, v254, 48
	v_readlane_b32 s47, v254, 49
	v_readlane_b32 s48, v254, 50
	v_readlane_b32 s49, v254, 51
.LBB0_1568:
	s_or_b64 exec, exec, s[28:29]
	s_waitcnt vmcnt(0)
	v_readfirstlane_b32 s6, v67
	s_nop 1
	v_add_u32_e32 v66, s6, v66
	v_add_u32_e32 v66, 0x340, v66

.LBB0_1570:
	s_or_b64 exec, exec, s[2:3]
	v_mov_b32_e32 v66, s25
	s_waitcnt lgkmcnt(0)
	s_waitcnt lgkmcnt(0)
	s_barrier
	ds_read_b32 v66, v66
	s_movk_i32 s2, 0x67f
	s_mov_b64 s[86:87], s[84:85]
	s_mov_b32 s53, s26
	s_mov_b32 s55, s33
	s_waitcnt lgkmcnt(0)
	v_cmp_lt_i32_e64 s[2:3], s2, v66
	v_readfirstlane_b32 s31, v66
	s_and_b64 vcc, exec, s[2:3]
	s_mov_b32 s54, s27
	s_mov_b32 s60, s82
	s_mov_b32 s88, s52
	s_mov_b32 s58, s59
	s_cbranch_vccnz .LBB0_1597
	s_cmpk_gt_i32 s31, 0x67f
	s_mov_b64 s[28:29], -1
	s_cbranch_scc0 .LBB0_1582
	s_cmpk_gt_u32 s31, 0xa9f
	s_cbranch_scc0 .LBB0_1575
	s_add_i32 s61, s31, 0xfffff560
	s_cmpk_lt_u32 s61, 0x1c0
	s_cbranch_scc1 .LBB0_1580
	v_readlane_b32 s36, v254, 38
	v_readlane_b32 s44, v254, 46
	v_readlane_b32 s45, v254, 47
	s_add_i32 s61, s31, 0xfffff3a0
	s_mov_b32 s54, 1
	v_readlane_b32 s37, v254, 39
	v_readlane_b32 s38, v254, 40
	v_readlane_b32 s39, v254, 41
	v_readlane_b32 s40, v254, 42
	v_readlane_b32 s41, v254, 43
	v_readlane_b32 s42, v254, 44
	v_readlane_b32 s43, v254, 45
	v_readlane_b32 s46, v254, 48
	v_readlane_b32 s47, v254, 49
	v_readlane_b32 s48, v254, 50
	v_readlane_b32 s49, v254, 51
	v_readlane_b32 s50, v254, 52
	v_readlane_b32 s51, v254, 53
	s_mov_b64 s[34:35], s[44:45]
	s_mov_b64 s[28:29], 0

.LBB0_2054:
	s_or_b64 exec, exec, s[6:7]
	s_waitcnt vmcnt(0)
	v_readfirstlane_b32 s6, v3
	s_nop 1
	v_add_u32_e32 v2, s6, v2
	s_add_i32 s6, 0, 0x20180
	v_add_u32_e32 v2, 0x1690, v2
	v_mov_b32_e32 v3, s6
	ds_write_b32 v3, v2

.LBB0_2120:
	s_or_b64 exec, exec, s[28:29]
	s_waitcnt vmcnt(0)
	v_readfirstlane_b32 s22, v67
	s_nop 1
	v_add_u32_e32 v66, s22, v66
	v_add_u32_e32 v66, 0x1690, v66

.LBB0_2296:
	s_or_b64 exec, exec, s[4:5]
	s_waitcnt vmcnt(0)
	v_readfirstlane_b32 s4, v3
	s_nop 1
	v_add_u32_e32 v2, s4, v2
	s_add_i32 s4, 0, 0x20180
	v_add_u32_e32 v2, 0x1690, v2
	v_mov_b32_e32 v3, s4
	ds_write_b32 v3, v2

.LBB0_2361:
	s_or_b64 exec, exec, s[28:29]
	s_waitcnt vmcnt(0)
	v_readfirstlane_b32 s18, v67
	s_nop 1
	v_add_u32_e32 v66, s18, v66
	v_add_u32_e32 v66, 0x1690, v66

.LBB0_2655:
	s_or_b64 exec, exec, s[28:29]
	s_waitcnt vmcnt(0)
	v_readfirstlane_b32 s18, v67
	s_nop 1
	v_add_u32_e32 v66, s18, v66
	v_add_u32_e32 v66, 0x1690, v66
	s_branch .LBB0_2657
